# fp8 GEMM K-loops (P4a/P4b/P5): the compiler's full VMEM drain in front of the loop removed (the loop's own counted waits and barriers cover the LDS-DMA protocol; epilogue stores drain in the backgroun
# speedup vs baseline: 1.0017x; 1.0017x over previous
.LBB0_991:
	s_ashr_i32 s15, s14, 31
	s_lshl_b64 s[16:17], s[14:15], 19
	v_readlane_b32 s18, v254, 45
	v_readlane_b32 s19, v254, 46
	s_add_u32 s16, s18, s16
	s_addc_u32 s17, s19, s17
	s_and_b64 s[18:19], s[0:1], exec
	s_cselect_b32 s15, s17, s23
	s_cselect_b32 s42, s16, s22
	s_ashr_i32 s13, s12, 31
	s_lshl_b64 s[18:19], s[12:13], 19
	v_readlane_b32 s13, v254, 39
	s_add_u32 s18, s13, s18
	v_readlane_b32 s13, v254, 40
	s_addc_u32 s19, s13, s19
	s_and_b64 s[26:27], s[0:1], exec
	s_cselect_b32 s13, s19, s25
	s_cselect_b32 s43, s18, s24
	s_add_u32 s22, s22, 0x40080
	s_addc_u32 s23, s23, 0
	s_add_u32 s44, s24, 0x100
	v_mov_b32_e32 v34, 0
	s_addc_u32 s45, s25, 0
	s_mov_b32 s46, -2
	v_mov_b32_e32 v35, v34
	v_mov_b32_e32 v36, v34
	v_mov_b32_e32 v37, v34
	v_mov_b32_e32 v38, v34
	v_mov_b32_e32 v39, v34
	v_mov_b32_e32 v40, v34
	v_mov_b32_e32 v41, v34
	v_mov_b32_e32 v50, v34
	v_mov_b32_e32 v51, v34
	v_mov_b32_e32 v52, v34
	v_mov_b32_e32 v53, v34
	v_mov_b32_e32 v54, v34
	v_mov_b32_e32 v55, v34
	v_mov_b32_e32 v56, v34
	v_mov_b32_e32 v57, v34
	v_mov_b32_e32 v66, v34
	v_mov_b32_e32 v67, v34
	v_mov_b32_e32 v68, v34
	v_mov_b32_e32 v69, v34
	v_mov_b32_e32 v70, v34
	v_mov_b32_e32 v71, v34
	v_mov_b32_e32 v72, v34
	v_mov_b32_e32 v73, v34
	v_mov_b32_e32 v82, v34
	v_mov_b32_e32 v83, v34
	v_mov_b32_e32 v84, v34
	v_mov_b32_e32 v85, v34
	v_mov_b32_e32 v86, v34
	v_mov_b32_e32 v87, v34
	v_mov_b32_e32 v88, v34
	v_mov_b32_e32 v89, v34
	v_mov_b32_e32 v42, v34
	v_mov_b32_e32 v43, v34
	v_mov_b32_e32 v44, v34
	v_mov_b32_e32 v45, v34
	v_mov_b32_e32 v46, v34
	v_mov_b32_e32 v47, v34
	v_mov_b32_e32 v48, v34
	v_mov_b32_e32 v49, v34
	v_mov_b32_e32 v58, v34
	v_mov_b32_e32 v59, v34
	v_mov_b32_e32 v60, v34
	v_mov_b32_e32 v61, v34
	v_mov_b32_e32 v62, v34
	v_mov_b32_e32 v63, v34
	v_mov_b32_e32 v64, v34
	v_mov_b32_e32 v65, v34
	v_mov_b32_e32 v74, v34
	v_mov_b32_e32 v75, v34
	v_mov_b32_e32 v76, v34
	v_mov_b32_e32 v77, v34
	v_mov_b32_e32 v78, v34
	v_mov_b32_e32 v79, v34
	v_mov_b32_e32 v80, v34
	v_mov_b32_e32 v81, v34
	v_mov_b32_e32 v90, v34
	v_mov_b32_e32 v91, v34
	v_mov_b32_e32 v92, v34
	v_mov_b32_e32 v93, v34
	v_mov_b32_e32 v94, v34
	v_mov_b32_e32 v95, v34
	v_mov_b32_e32 v96, v34
	v_mov_b32_e32 v97, v34
	v_mov_b32_e32 v98, v34
	v_mov_b32_e32 v99, v34
	v_mov_b32_e32 v100, v34
	v_mov_b32_e32 v101, v34
	v_mov_b32_e32 v102, v34
	v_mov_b32_e32 v103, v34
	v_mov_b32_e32 v104, v34
	v_mov_b32_e32 v105, v34
	v_mov_b32_e32 v114, v34
	v_mov_b32_e32 v115, v34
	v_mov_b32_e32 v116, v34
	v_mov_b32_e32 v117, v34
	v_mov_b32_e32 v118, v34
	v_mov_b32_e32 v119, v34
	v_mov_b32_e32 v120, v34
	v_mov_b32_e32 v121, v34
	v_mov_b32_e32 v130, v34
	v_mov_b32_e32 v131, v34
	v_mov_b32_e32 v132, v34
	v_mov_b32_e32 v133, v34
	v_mov_b32_e32 v134, v34
	v_mov_b32_e32 v135, v34
	v_mov_b32_e32 v136, v34
	v_mov_b32_e32 v137, v34
	v_mov_b32_e32 v146, v34
	v_mov_b32_e32 v147, v34
	v_mov_b32_e32 v148, v34
	v_mov_b32_e32 v149, v34
	v_mov_b32_e32 v150, v34
	v_mov_b32_e32 v151, v34
	v_mov_b32_e32 v152, v34
	v_mov_b32_e32 v153, v34
	v_mov_b32_e32 v106, v34
	v_mov_b32_e32 v107, v34
	v_mov_b32_e32 v108, v34
	v_mov_b32_e32 v109, v34
	v_mov_b32_e32 v110, v34
	v_mov_b32_e32 v111, v34
	v_mov_b32_e32 v112, v34
	v_mov_b32_e32 v113, v34
	v_mov_b32_e32 v122, v34
	v_mov_b32_e32 v123, v34
	v_mov_b32_e32 v124, v34
	v_mov_b32_e32 v125, v34
	v_mov_b32_e32 v126, v34
	v_mov_b32_e32 v127, v34
	v_mov_b32_e32 v128, v34
	v_mov_b32_e32 v129, v34
	v_mov_b32_e32 v138, v34
	v_mov_b32_e32 v139, v34
	v_mov_b32_e32 v140, v34
	v_mov_b32_e32 v141, v34
	v_mov_b32_e32 v142, v34
	v_mov_b32_e32 v143, v34
	v_mov_b32_e32 v144, v34
	v_mov_b32_e32 v145, v34
	v_mov_b32_e32 v154, v34
	v_mov_b32_e32 v155, v34
	v_mov_b32_e32 v156, v34
	v_mov_b32_e32 v157, v34
	v_mov_b32_e32 v158, v34
	v_mov_b32_e32 v159, v34
	v_mov_b32_e32 v160, v34
	v_mov_b32_e32 v161, v34
.LBB0_992:
	ds_read_b128 v[26:29], v199
	ds_read_b128 v[30:33], v199 offset:1024
	ds_read_b128 v[18:21], v199 offset:2048
	ds_read_b128 v[22:25], v199 offset:3072
	ds_read_b128 v[10:13], v200
	ds_read_b128 v[14:17], v200 offset:1024
	ds_read_b128 v[2:5], v200 offset:2048
	ds_read_b128 v[6:9], v200 offset:3072
	s_add_u32 s24, s22, 0xfffc0080
	s_addc_u32 s25, s23, -1
	s_cmp_eq_u32 s46, 12
	s_cselect_b32 s27, s15, s25
	s_cselect_b32 s26, s42, s24
	s_cselect_b32 s25, s13, s45
	s_cselect_b32 s24, s43, s44
	v_lshl_add_u64 v[218:219], s[22:23], 0, v[170:171]
	s_add_i32 m0, s21, 0xc000
	ds_read_b128 v[180:183], v201
	ds_read_b128 v[184:187], v201 offset:1024
	ds_read_b128 v[202:205], v201 offset:2048
	ds_read_b128 v[206:209], v201 offset:3072
	ds_read_b128 v[210:213], v201 offset:4096
	ds_read_b128 v[214:217], v201 offset:5120
	ds_read_b128 v[224:227], v201 offset:6144
	ds_read_b128 v[228:231], v201 offset:7168
	global_load_lds_dwordx4 v[218:219], off
	v_lshl_add_u64 v[218:219], s[22:23], 0, v[172:173]
	s_add_i32 m0, s21, 0xe000
	s_nop 0
	global_load_lds_dwordx4 v[218:219], off
	s_waitcnt vmcnt(8)
	s_waitcnt lgkmcnt(0)
	s_barrier
	s_setprio 1
	s_waitcnt lgkmcnt(0)
	v_mfma_f32_16x16x128_f8f6f4 v[158:161], v[26:33], v[180:187], v[158:161]
	v_mfma_f32_16x16x128_f8f6f4 v[154:157], v[18:25], v[180:187], v[154:157]
	v_mfma_f32_16x16x128_f8f6f4 v[142:145], v[26:33], v[202:209], v[142:145]
	v_mfma_f32_16x16x128_f8f6f4 v[138:141], v[18:25], v[202:209], v[138:141]
	v_mfma_f32_16x16x128_f8f6f4 v[126:129], v[26:33], v[210:217], v[126:129]
	v_mfma_f32_16x16x128_f8f6f4 v[122:125], v[18:25], v[210:217], v[122:125]
	v_mfma_f32_16x16x128_f8f6f4 v[110:113], v[26:33], v[224:231], v[110:113]
	v_mfma_f32_16x16x128_f8f6f4 v[106:109], v[18:25], v[224:231], v[106:109]
	s_setprio 0
	s_setprio 1
	v_mfma_f32_16x16x128_f8f6f4 v[150:153], v[10:17], v[180:187], v[150:153]
	v_mfma_f32_16x16x128_f8f6f4 v[146:149], v[2:9], v[180:187], v[146:149]
	v_mfma_f32_16x16x128_f8f6f4 v[134:137], v[10:17], v[202:209], v[134:137]
	v_mfma_f32_16x16x128_f8f6f4 v[130:133], v[2:9], v[202:209], v[130:133]
	v_mfma_f32_16x16x128_f8f6f4 v[118:121], v[10:17], v[210:217], v[118:121]
	v_mfma_f32_16x16x128_f8f6f4 v[114:117], v[2:9], v[210:217], v[114:117]
	v_mfma_f32_16x16x128_f8f6f4 v[102:105], v[10:17], v[224:231], v[102:105]
	v_mfma_f32_16x16x128_f8f6f4 v[98:101], v[2:9], v[224:231], v[98:101]
	s_setprio 0
	s_barrier
	s_add_i32 s47, s36, s3
	v_lshl_add_u64 v[180:181], s[24:25], 0, v[164:165]
	s_mov_b32 m0, s47
	ds_read_b128 v[202:205], v201 offset:16384
	ds_read_b128 v[206:209], v201 offset:17408
	ds_read_b128 v[210:213], v201 offset:18432
	ds_read_b128 v[214:217], v201 offset:19456
	ds_read_b128 v[224:227], v201 offset:20480
	ds_read_b128 v[228:231], v201 offset:21504
	ds_read_b128 v[232:235], v201 offset:22528
	ds_read_b128 v[236:239], v201 offset:23552
	global_load_lds_dwordx4 v[180:181], off
	s_add_i32 m0, s47, 0x2000
	s_add_u32 s48, s24, 0x40000
	v_lshl_add_u64 v[182:183], s[24:25], 0, v[168:169]
	s_addc_u32 s49, s25, 0
	s_add_i32 s47, s37, s3
	global_load_lds_dwordx4 v[182:183], off
	v_lshl_add_u64 v[184:185], s[48:49], 0, v[164:165]
	s_mov_b32 m0, s47
	v_lshl_add_u64 v[186:187], s[26:27], 0, v[166:167]
	global_load_lds_dwordx4 v[184:185], off
	v_lshl_add_u64 v[184:185], s[48:49], 0, v[168:169]
	s_add_i32 m0, s47, 0x2000
	s_nop 0
	global_load_lds_dwordx4 v[184:185], off
	v_lshl_add_u64 v[184:185], s[26:27], 0, v[162:163]
	s_mov_b32 m0, s21
	s_nop 0
	global_load_lds_dwordx4 v[184:185], off
	s_mov_b32 m0, s28
	s_nop 0
	global_load_lds_dwordx4 v[186:187], off
	s_waitcnt vmcnt(8)
	s_waitcnt lgkmcnt(0)
	s_barrier
	s_setprio 1
	s_waitcnt lgkmcnt(0)
	v_mfma_f32_16x16x128_f8f6f4 v[94:97], v[26:33], v[202:209], v[94:97]
	v_mfma_f32_16x16x128_f8f6f4 v[90:93], v[18:25], v[202:209], v[90:93]
	v_mfma_f32_16x16x128_f8f6f4 v[78:81], v[26:33], v[210:217], v[78:81]
	v_mfma_f32_16x16x128_f8f6f4 v[74:77], v[18:25], v[210:217], v[74:77]
	v_mfma_f32_16x16x128_f8f6f4 v[62:65], v[26:33], v[224:231], v[62:65]
	v_mfma_f32_16x16x128_f8f6f4 v[58:61], v[18:25], v[224:231], v[58:61]
	v_mfma_f32_16x16x128_f8f6f4 v[46:49], v[26:33], v[232:239], v[46:49]
	v_mfma_f32_16x16x128_f8f6f4 v[42:45], v[18:25], v[232:239], v[42:45]
	s_setprio 0
	s_setprio 1
	v_mfma_f32_16x16x128_f8f6f4 v[86:89], v[10:17], v[202:209], v[86:89]
	v_mfma_f32_16x16x128_f8f6f4 v[82:85], v[2:9], v[202:209], v[82:85]
	v_mfma_f32_16x16x128_f8f6f4 v[70:73], v[10:17], v[210:217], v[70:73]
	v_mfma_f32_16x16x128_f8f6f4 v[66:69], v[2:9], v[210:217], v[66:69]
	v_mfma_f32_16x16x128_f8f6f4 v[54:57], v[10:17], v[224:231], v[54:57]
	v_mfma_f32_16x16x128_f8f6f4 v[50:53], v[2:9], v[224:231], v[50:53]
	v_mfma_f32_16x16x128_f8f6f4 v[38:41], v[10:17], v[232:239], v[38:41]
	v_mfma_f32_16x16x128_f8f6f4 v[34:37], v[2:9], v[232:239], v[34:37]
	s_setprio 0
	s_barrier
	s_add_i32 s47, 0, 0x18000
	s_add_i32 s48, 0, 0x1c000
	v_add_u32_e32 v14, s47, v197
	v_add_u32_e32 v30, s48, v197
	ds_read_b128 v[2:5], v14
	ds_read_b128 v[6:9], v14 offset:1024
	ds_read_b128 v[10:13], v14 offset:2048
	ds_read_b128 v[14:17], v14 offset:3072
	ds_read_b128 v[18:21], v30
	ds_read_b128 v[22:25], v30 offset:1024
	ds_read_b128 v[26:29], v30 offset:2048
	ds_read_b128 v[30:33], v30 offset:3072
	s_add_u32 s26, s26, 0x40000
	s_addc_u32 s27, s27, 0
	s_mov_b32 m0, s29
	v_lshl_add_u64 v[218:219], s[26:27], 0, v[162:163]
	ds_read_b128 v[202:205], v201 offset:32768
	ds_read_b128 v[206:209], v201 offset:33792
	ds_read_b128 v[210:213], v201 offset:34816
	ds_read_b128 v[214:217], v201 offset:35840
	ds_read_b128 v[224:227], v201 offset:36864
	ds_read_b128 v[228:231], v201 offset:37888
	ds_read_b128 v[232:235], v201 offset:38912
	ds_read_b128 v[236:239], v201 offset:39936
	global_load_lds_dwordx4 v[218:219], off
	v_lshl_add_u64 v[218:219], s[26:27], 0, v[166:167]
	s_mov_b32 m0, s30
	s_nop 0
	global_load_lds_dwordx4 v[218:219], off
	s_waitcnt vmcnt(8)
	s_waitcnt lgkmcnt(0)
	s_barrier
	s_setprio 1
	s_waitcnt lgkmcnt(0)
	v_mfma_f32_16x16x128_f8f6f4 v[158:161], v[2:9], v[202:209], v[158:161]
	v_mfma_f32_16x16x128_f8f6f4 v[154:157], v[10:17], v[202:209], v[154:157]
	v_mfma_f32_16x16x128_f8f6f4 v[142:145], v[2:9], v[210:217], v[142:145]
	v_mfma_f32_16x16x128_f8f6f4 v[138:141], v[10:17], v[210:217], v[138:141]
	v_mfma_f32_16x16x128_f8f6f4 v[126:129], v[2:9], v[224:231], v[126:129]
	v_mfma_f32_16x16x128_f8f6f4 v[122:125], v[10:17], v[224:231], v[122:125]
	v_mfma_f32_16x16x128_f8f6f4 v[110:113], v[2:9], v[232:239], v[110:113]
	v_mfma_f32_16x16x128_f8f6f4 v[106:109], v[10:17], v[232:239], v[106:109]
	s_setprio 0
	s_setprio 1
	v_mfma_f32_16x16x128_f8f6f4 v[150:153], v[18:25], v[202:209], v[150:153]
	v_mfma_f32_16x16x128_f8f6f4 v[146:149], v[26:33], v[202:209], v[146:149]
	v_mfma_f32_16x16x128_f8f6f4 v[134:137], v[18:25], v[210:217], v[134:137]
	v_mfma_f32_16x16x128_f8f6f4 v[130:133], v[26:33], v[210:217], v[130:133]
	v_mfma_f32_16x16x128_f8f6f4 v[118:121], v[18:25], v[224:231], v[118:121]
	v_mfma_f32_16x16x128_f8f6f4 v[114:117], v[26:33], v[224:231], v[114:117]
	v_mfma_f32_16x16x128_f8f6f4 v[102:105], v[18:25], v[232:239], v[102:105]
	v_mfma_f32_16x16x128_f8f6f4 v[98:101], v[26:33], v[232:239], v[98:101]
	s_setprio 0
	s_barrier
	s_add_i32 s26, s47, s3
	v_lshl_add_u64 v[180:181], v[180:181], 0, s[8:9]
	s_mov_b32 m0, s26
	ds_read_b128 v[202:205], v201 offset:49152
	ds_read_b128 v[206:209], v201 offset:50176
	ds_read_b128 v[210:213], v201 offset:51200
	ds_read_b128 v[214:217], v201 offset:52224
	ds_read_b128 v[224:227], v201 offset:53248
	ds_read_b128 v[228:231], v201 offset:54272
	ds_read_b128 v[232:235], v201 offset:55296
	ds_read_b128 v[236:239], v201 offset:56320
	global_load_lds_dwordx4 v[180:181], off
	s_add_i32 m0, s26, 0x2000
	s_add_u32 s24, s24, 0x40080
	v_lshl_add_u64 v[180:181], v[182:183], 0, s[8:9]
	s_addc_u32 s25, s25, 0
	s_add_i32 s26, s48, s3
	global_load_lds_dwordx4 v[180:181], off
	v_lshl_add_u64 v[180:181], s[24:25], 0, v[164:165]
	s_mov_b32 m0, s26
	s_nop 0
	global_load_lds_dwordx4 v[180:181], off
	v_lshl_add_u64 v[180:181], s[24:25], 0, v[168:169]
	s_add_i32 m0, s26, 0x2000
	s_nop 0
	global_load_lds_dwordx4 v[180:181], off
	v_lshl_add_u64 v[180:181], v[184:185], 0, s[8:9]
	s_mov_b32 m0, s33
	s_nop 0
	global_load_lds_dwordx4 v[180:181], off
	v_lshl_add_u64 v[180:181], v[186:187], 0, s[8:9]
	s_mov_b32 m0, s34
	s_nop 0
	global_load_lds_dwordx4 v[180:181], off
	s_waitcnt vmcnt(8)
	s_waitcnt lgkmcnt(0)
	s_barrier
	s_setprio 1
	s_waitcnt lgkmcnt(0)
	v_mfma_f32_16x16x128_f8f6f4 v[94:97], v[2:9], v[202:209], v[94:97]
	v_mfma_f32_16x16x128_f8f6f4 v[90:93], v[10:17], v[202:209], v[90:93]
	v_mfma_f32_16x16x128_f8f6f4 v[78:81], v[2:9], v[210:217], v[78:81]
	v_mfma_f32_16x16x128_f8f6f4 v[74:77], v[10:17], v[210:217], v[74:77]
	v_mfma_f32_16x16x128_f8f6f4 v[62:65], v[2:9], v[224:231], v[62:65]
	v_mfma_f32_16x16x128_f8f6f4 v[58:61], v[10:17], v[224:231], v[58:61]
	v_mfma_f32_16x16x128_f8f6f4 v[46:49], v[2:9], v[232:239], v[46:49]
	v_mfma_f32_16x16x128_f8f6f4 v[42:45], v[10:17], v[232:239], v[42:45]
	s_setprio 0
	s_setprio 1
	v_mfma_f32_16x16x128_f8f6f4 v[86:89], v[18:25], v[202:209], v[86:89]
	v_mfma_f32_16x16x128_f8f6f4 v[82:85], v[26:33], v[202:209], v[82:85]
	v_mfma_f32_16x16x128_f8f6f4 v[70:73], v[18:25], v[210:217], v[70:73]
	v_mfma_f32_16x16x128_f8f6f4 v[66:69], v[26:33], v[210:217], v[66:69]
	v_mfma_f32_16x16x128_f8f6f4 v[54:57], v[18:25], v[224:231], v[54:57]
	v_mfma_f32_16x16x128_f8f6f4 v[50:53], v[26:33], v[224:231], v[50:53]
	v_mfma_f32_16x16x128_f8f6f4 v[38:41], v[18:25], v[232:239], v[38:41]
	v_mfma_f32_16x16x128_f8f6f4 v[34:37], v[26:33], v[232:239], v[34:37]
	s_setprio 0
	s_barrier
	s_add_i32 s46, s46, 2
	s_add_u32 s22, s22, 0x100
	s_addc_u32 s23, s23, 0
	s_add_u32 s44, s44, 0x100
	s_addc_u32 s45, s45, 0
	s_cmp_gt_u32 s46, 13
	s_cbranch_scc0 .LBB0_992
	s_and_b64 vcc, exec, s[10:11]
	s_cbranch_vccz .LBB0_995
	s_barrier

.LBB0_1015:
	s_ashr_i32 s11, s10, 31
	s_lshl_b64 s[12:13], s[10:11], 19
	s_add_u32 s12, s25, s12
	s_addc_u32 s13, s26, s13
	s_and_b64 s[14:15], s[0:1], exec
	s_cselect_b32 s11, s13, s19
	s_cselect_b32 s43, s12, s18
	s_ashr_i32 s9, s8, 31
	s_lshl_b64 s[14:15], s[8:9], 19
	v_readlane_b32 s9, v254, 42
	s_add_u32 s14, s9, s14
	v_readlane_b32 s9, v254, 43
	s_addc_u32 s15, s9, s15
	s_and_b64 s[22:23], s[0:1], exec
	s_cselect_b32 s9, s15, s21
	s_cselect_b32 s44, s14, s20
	s_add_u32 s18, s18, 0x40080
	s_addc_u32 s19, s19, 0
	s_add_u32 s45, s20, 0x100
	v_mov_b32_e32 v34, 0
	s_addc_u32 s46, s21, 0
	s_mov_b32 s47, -2
	v_mov_b32_e32 v35, v34
	v_mov_b32_e32 v36, v34
	v_mov_b32_e32 v37, v34
	v_mov_b32_e32 v38, v34
	v_mov_b32_e32 v39, v34
	v_mov_b32_e32 v40, v34
	v_mov_b32_e32 v41, v34
	v_mov_b32_e32 v50, v34
	v_mov_b32_e32 v51, v34
	v_mov_b32_e32 v52, v34
	v_mov_b32_e32 v53, v34
	v_mov_b32_e32 v54, v34
	v_mov_b32_e32 v55, v34
	v_mov_b32_e32 v56, v34
	v_mov_b32_e32 v57, v34
	v_mov_b32_e32 v66, v34
	v_mov_b32_e32 v67, v34
	v_mov_b32_e32 v68, v34
	v_mov_b32_e32 v69, v34
	v_mov_b32_e32 v70, v34
	v_mov_b32_e32 v71, v34
	v_mov_b32_e32 v72, v34
	v_mov_b32_e32 v73, v34
	v_mov_b32_e32 v82, v34
	v_mov_b32_e32 v83, v34
	v_mov_b32_e32 v84, v34
	v_mov_b32_e32 v85, v34
	v_mov_b32_e32 v86, v34
	v_mov_b32_e32 v87, v34
	v_mov_b32_e32 v88, v34
	v_mov_b32_e32 v89, v34
	v_mov_b32_e32 v42, v34
	v_mov_b32_e32 v43, v34
	v_mov_b32_e32 v44, v34
	v_mov_b32_e32 v45, v34
	v_mov_b32_e32 v46, v34
	v_mov_b32_e32 v47, v34
	v_mov_b32_e32 v48, v34
	v_mov_b32_e32 v49, v34
	v_mov_b32_e32 v58, v34
	v_mov_b32_e32 v59, v34
	v_mov_b32_e32 v60, v34
	v_mov_b32_e32 v61, v34
	v_mov_b32_e32 v62, v34
	v_mov_b32_e32 v63, v34
	v_mov_b32_e32 v64, v34
	v_mov_b32_e32 v65, v34
	v_mov_b32_e32 v74, v34
	v_mov_b32_e32 v75, v34
	v_mov_b32_e32 v76, v34
	v_mov_b32_e32 v77, v34
	v_mov_b32_e32 v78, v34
	v_mov_b32_e32 v79, v34
	v_mov_b32_e32 v80, v34
	v_mov_b32_e32 v81, v34
	v_mov_b32_e32 v90, v34
	v_mov_b32_e32 v91, v34
	v_mov_b32_e32 v92, v34
	v_mov_b32_e32 v93, v34
	v_mov_b32_e32 v94, v34
	v_mov_b32_e32 v95, v34
	v_mov_b32_e32 v96, v34
	v_mov_b32_e32 v97, v34
	v_mov_b32_e32 v98, v34
	v_mov_b32_e32 v99, v34
	v_mov_b32_e32 v100, v34
	v_mov_b32_e32 v101, v34
	v_mov_b32_e32 v102, v34
	v_mov_b32_e32 v103, v34
	v_mov_b32_e32 v104, v34
	v_mov_b32_e32 v105, v34
	v_mov_b32_e32 v114, v34
	v_mov_b32_e32 v115, v34
	v_mov_b32_e32 v116, v34
	v_mov_b32_e32 v117, v34
	v_mov_b32_e32 v118, v34
	v_mov_b32_e32 v119, v34
	v_mov_b32_e32 v120, v34
	v_mov_b32_e32 v121, v34
	v_mov_b32_e32 v130, v34
	v_mov_b32_e32 v131, v34
	v_mov_b32_e32 v132, v34
	v_mov_b32_e32 v133, v34
	v_mov_b32_e32 v134, v34
	v_mov_b32_e32 v135, v34
	v_mov_b32_e32 v136, v34
	v_mov_b32_e32 v137, v34
	v_mov_b32_e32 v146, v34
	v_mov_b32_e32 v147, v34
	v_mov_b32_e32 v148, v34
	v_mov_b32_e32 v149, v34
	v_mov_b32_e32 v150, v34
	v_mov_b32_e32 v151, v34
	v_mov_b32_e32 v152, v34
	v_mov_b32_e32 v153, v34
	v_mov_b32_e32 v106, v34
	v_mov_b32_e32 v107, v34
	v_mov_b32_e32 v108, v34
	v_mov_b32_e32 v109, v34
	v_mov_b32_e32 v110, v34
	v_mov_b32_e32 v111, v34
	v_mov_b32_e32 v112, v34
	v_mov_b32_e32 v113, v34
	v_mov_b32_e32 v122, v34
	v_mov_b32_e32 v123, v34
	v_mov_b32_e32 v124, v34
	v_mov_b32_e32 v125, v34
	v_mov_b32_e32 v126, v34
	v_mov_b32_e32 v127, v34
	v_mov_b32_e32 v128, v34
	v_mov_b32_e32 v129, v34
	v_mov_b32_e32 v138, v34
	v_mov_b32_e32 v139, v34
	v_mov_b32_e32 v140, v34
	v_mov_b32_e32 v141, v34
	v_mov_b32_e32 v142, v34
	v_mov_b32_e32 v143, v34
	v_mov_b32_e32 v144, v34
	v_mov_b32_e32 v145, v34
	v_mov_b32_e32 v154, v34
	v_mov_b32_e32 v155, v34
	v_mov_b32_e32 v156, v34
	v_mov_b32_e32 v157, v34
	v_mov_b32_e32 v158, v34
	v_mov_b32_e32 v159, v34
	v_mov_b32_e32 v160, v34
	v_mov_b32_e32 v161, v34
.LBB0_1016:
	ds_read_b128 v[26:29], v188
	ds_read_b128 v[30:33], v188 offset:1024
	ds_read_b128 v[18:21], v188 offset:2048
	ds_read_b128 v[22:25], v188 offset:3072
	ds_read_b128 v[10:13], v189
	ds_read_b128 v[14:17], v189 offset:1024
	ds_read_b128 v[2:5], v189 offset:2048
	ds_read_b128 v[6:9], v189 offset:3072
	s_add_u32 s20, s18, 0xfffc0080
	s_addc_u32 s21, s19, -1
	s_cmp_eq_u32 s47, 12
	s_cselect_b32 s23, s11, s21
	s_cselect_b32 s22, s43, s20
	s_cselect_b32 s21, s9, s46
	s_cselect_b32 s20, s44, s45
	v_lshl_add_u64 v[194:195], s[18:19], 0, v[170:171]
	s_add_i32 m0, s17, 0xc000
	ds_read_b128 v[180:183], v190
	ds_read_b128 v[184:187], v190 offset:1024
	ds_read_b128 v[198:201], v190 offset:2048
	ds_read_b128 v[202:205], v190 offset:3072
	ds_read_b128 v[206:209], v190 offset:4096
	ds_read_b128 v[210:213], v190 offset:5120
	ds_read_b128 v[224:227], v190 offset:6144
	ds_read_b128 v[228:231], v190 offset:7168
	global_load_lds_dwordx4 v[194:195], off
	v_lshl_add_u64 v[194:195], s[18:19], 0, v[172:173]
	s_add_i32 m0, s17, 0xe000
	s_nop 0
	global_load_lds_dwordx4 v[194:195], off
	s_waitcnt vmcnt(8)
	s_waitcnt lgkmcnt(0)
	s_barrier
	s_setprio 1
	s_waitcnt lgkmcnt(0)
	v_mfma_f32_16x16x128_f8f6f4 v[158:161], v[26:33], v[180:187], v[158:161]
	v_mfma_f32_16x16x128_f8f6f4 v[154:157], v[18:25], v[180:187], v[154:157]
	v_mfma_f32_16x16x128_f8f6f4 v[142:145], v[26:33], v[198:205], v[142:145]
	v_mfma_f32_16x16x128_f8f6f4 v[138:141], v[18:25], v[198:205], v[138:141]
	v_mfma_f32_16x16x128_f8f6f4 v[126:129], v[26:33], v[206:213], v[126:129]
	v_mfma_f32_16x16x128_f8f6f4 v[122:125], v[18:25], v[206:213], v[122:125]
	v_mfma_f32_16x16x128_f8f6f4 v[110:113], v[26:33], v[224:231], v[110:113]
	v_mfma_f32_16x16x128_f8f6f4 v[106:109], v[18:25], v[224:231], v[106:109]
	s_setprio 0
	s_setprio 1
	v_mfma_f32_16x16x128_f8f6f4 v[150:153], v[10:17], v[180:187], v[150:153]
	v_mfma_f32_16x16x128_f8f6f4 v[146:149], v[2:9], v[180:187], v[146:149]
	v_mfma_f32_16x16x128_f8f6f4 v[134:137], v[10:17], v[198:205], v[134:137]
	v_mfma_f32_16x16x128_f8f6f4 v[130:133], v[2:9], v[198:205], v[130:133]
	v_mfma_f32_16x16x128_f8f6f4 v[118:121], v[10:17], v[206:213], v[118:121]
	v_mfma_f32_16x16x128_f8f6f4 v[114:117], v[2:9], v[206:213], v[114:117]
	v_mfma_f32_16x16x128_f8f6f4 v[102:105], v[10:17], v[224:231], v[102:105]
	v_mfma_f32_16x16x128_f8f6f4 v[98:101], v[2:9], v[224:231], v[98:101]
	s_setprio 0
	s_barrier
	s_add_i32 s48, s38, s27
	v_lshl_add_u64 v[180:181], s[20:21], 0, v[164:165]
	s_mov_b32 m0, s48
	ds_read_b128 v[198:201], v190 offset:16384
	ds_read_b128 v[202:205], v190 offset:17408
	ds_read_b128 v[206:209], v190 offset:18432
	ds_read_b128 v[210:213], v190 offset:19456
	ds_read_b128 v[224:227], v190 offset:20480
	ds_read_b128 v[228:231], v190 offset:21504
	ds_read_b128 v[232:235], v190 offset:22528
	ds_read_b128 v[236:239], v190 offset:23552
	global_load_lds_dwordx4 v[180:181], off
	s_add_i32 m0, s48, 0x2000
	s_add_u32 s48, s20, 0x40000
	v_lshl_add_u64 v[182:183], s[20:21], 0, v[168:169]
	s_addc_u32 s49, s21, 0
	s_add_i32 s50, s39, s27
	global_load_lds_dwordx4 v[182:183], off
	v_lshl_add_u64 v[184:185], s[48:49], 0, v[164:165]
	s_mov_b32 m0, s50
	v_lshl_add_u64 v[186:187], s[22:23], 0, v[166:167]
	global_load_lds_dwordx4 v[184:185], off
	v_lshl_add_u64 v[184:185], s[48:49], 0, v[168:169]
	s_add_i32 m0, s50, 0x2000
	s_nop 0
	global_load_lds_dwordx4 v[184:185], off
	v_lshl_add_u64 v[184:185], s[22:23], 0, v[162:163]
	s_mov_b32 m0, s17
	s_nop 0
	global_load_lds_dwordx4 v[184:185], off
	s_mov_b32 m0, s28
	s_nop 0
	global_load_lds_dwordx4 v[186:187], off
	s_waitcnt vmcnt(8)
	s_waitcnt lgkmcnt(0)
	s_barrier
	s_setprio 1
	s_waitcnt lgkmcnt(0)
	v_mfma_f32_16x16x128_f8f6f4 v[94:97], v[26:33], v[198:205], v[94:97]
	v_mfma_f32_16x16x128_f8f6f4 v[90:93], v[18:25], v[198:205], v[90:93]
	v_mfma_f32_16x16x128_f8f6f4 v[78:81], v[26:33], v[206:213], v[78:81]
	v_mfma_f32_16x16x128_f8f6f4 v[74:77], v[18:25], v[206:213], v[74:77]
	v_mfma_f32_16x16x128_f8f6f4 v[62:65], v[26:33], v[224:231], v[62:65]
	v_mfma_f32_16x16x128_f8f6f4 v[58:61], v[18:25], v[224:231], v[58:61]
	v_mfma_f32_16x16x128_f8f6f4 v[46:49], v[26:33], v[232:239], v[46:49]
	v_mfma_f32_16x16x128_f8f6f4 v[42:45], v[18:25], v[232:239], v[42:45]
	s_setprio 0
	s_setprio 1
	v_mfma_f32_16x16x128_f8f6f4 v[86:89], v[10:17], v[198:205], v[86:89]
	v_mfma_f32_16x16x128_f8f6f4 v[82:85], v[2:9], v[198:205], v[82:85]
	v_mfma_f32_16x16x128_f8f6f4 v[70:73], v[10:17], v[206:213], v[70:73]
	v_mfma_f32_16x16x128_f8f6f4 v[66:69], v[2:9], v[206:213], v[66:69]
	v_mfma_f32_16x16x128_f8f6f4 v[54:57], v[10:17], v[224:231], v[54:57]
	v_mfma_f32_16x16x128_f8f6f4 v[50:53], v[2:9], v[224:231], v[50:53]
	v_mfma_f32_16x16x128_f8f6f4 v[38:41], v[10:17], v[232:239], v[38:41]
	v_mfma_f32_16x16x128_f8f6f4 v[34:37], v[2:9], v[232:239], v[34:37]
	s_setprio 0
	s_barrier
	s_add_i32 s48, 0, 0x18000
	s_add_i32 s49, 0, 0x1c000
	v_add_u32_e32 v14, s48, v193
	v_add_u32_e32 v30, s49, v193
	ds_read_b128 v[2:5], v14
	ds_read_b128 v[6:9], v14 offset:1024
	ds_read_b128 v[10:13], v14 offset:2048
	ds_read_b128 v[14:17], v14 offset:3072
	ds_read_b128 v[18:21], v30
	ds_read_b128 v[22:25], v30 offset:1024
	ds_read_b128 v[26:29], v30 offset:2048
	ds_read_b128 v[30:33], v30 offset:3072
	s_add_u32 s22, s22, 0x40000
	s_addc_u32 s23, s23, 0
	s_mov_b32 m0, s29
	v_lshl_add_u64 v[194:195], s[22:23], 0, v[162:163]
	ds_read_b128 v[198:201], v190 offset:32768
	ds_read_b128 v[202:205], v190 offset:33792
	ds_read_b128 v[206:209], v190 offset:34816
	ds_read_b128 v[210:213], v190 offset:35840
	ds_read_b128 v[224:227], v190 offset:36864
	ds_read_b128 v[228:231], v190 offset:37888
	ds_read_b128 v[232:235], v190 offset:38912
	ds_read_b128 v[236:239], v190 offset:39936
	global_load_lds_dwordx4 v[194:195], off
	v_lshl_add_u64 v[194:195], s[22:23], 0, v[166:167]
	s_mov_b32 m0, s30
	s_nop 0
	global_load_lds_dwordx4 v[194:195], off
	s_waitcnt vmcnt(8)
	s_waitcnt lgkmcnt(0)
	s_barrier
	s_setprio 1
	s_waitcnt lgkmcnt(0)
	v_mfma_f32_16x16x128_f8f6f4 v[158:161], v[2:9], v[198:205], v[158:161]
	v_mfma_f32_16x16x128_f8f6f4 v[154:157], v[10:17], v[198:205], v[154:157]
	v_mfma_f32_16x16x128_f8f6f4 v[142:145], v[2:9], v[206:213], v[142:145]
	v_mfma_f32_16x16x128_f8f6f4 v[138:141], v[10:17], v[206:213], v[138:141]
	v_mfma_f32_16x16x128_f8f6f4 v[126:129], v[2:9], v[224:231], v[126:129]
	v_mfma_f32_16x16x128_f8f6f4 v[122:125], v[10:17], v[224:231], v[122:125]
	v_mfma_f32_16x16x128_f8f6f4 v[110:113], v[2:9], v[232:239], v[110:113]
	v_mfma_f32_16x16x128_f8f6f4 v[106:109], v[10:17], v[232:239], v[106:109]
	s_setprio 0
	s_setprio 1
	v_mfma_f32_16x16x128_f8f6f4 v[150:153], v[18:25], v[198:205], v[150:153]
	v_mfma_f32_16x16x128_f8f6f4 v[146:149], v[26:33], v[198:205], v[146:149]
	v_mfma_f32_16x16x128_f8f6f4 v[134:137], v[18:25], v[206:213], v[134:137]
	v_mfma_f32_16x16x128_f8f6f4 v[130:133], v[26:33], v[206:213], v[130:133]
	v_mfma_f32_16x16x128_f8f6f4 v[118:121], v[18:25], v[224:231], v[118:121]
	v_mfma_f32_16x16x128_f8f6f4 v[114:117], v[26:33], v[224:231], v[114:117]
	v_mfma_f32_16x16x128_f8f6f4 v[102:105], v[18:25], v[232:239], v[102:105]
	v_mfma_f32_16x16x128_f8f6f4 v[98:101], v[26:33], v[232:239], v[98:101]
	s_setprio 0
	s_barrier
	s_add_i32 s22, s48, s27
	v_lshl_add_u64 v[180:181], v[180:181], 0, s[4:5]
	s_mov_b32 m0, s22
	ds_read_b128 v[198:201], v190 offset:49152
	ds_read_b128 v[202:205], v190 offset:50176
	ds_read_b128 v[206:209], v190 offset:51200
	ds_read_b128 v[210:213], v190 offset:52224
	ds_read_b128 v[224:227], v190 offset:53248
	ds_read_b128 v[228:231], v190 offset:54272
	ds_read_b128 v[232:235], v190 offset:55296
	ds_read_b128 v[236:239], v190 offset:56320
	global_load_lds_dwordx4 v[180:181], off
	s_add_i32 m0, s22, 0x2000
	s_add_u32 s20, s20, 0x40080
	v_lshl_add_u64 v[180:181], v[182:183], 0, s[4:5]
	s_addc_u32 s21, s21, 0
	s_add_i32 s22, s49, s27
	global_load_lds_dwordx4 v[180:181], off
	v_lshl_add_u64 v[180:181], s[20:21], 0, v[164:165]
	s_mov_b32 m0, s22
	s_nop 0
	global_load_lds_dwordx4 v[180:181], off
	v_lshl_add_u64 v[180:181], s[20:21], 0, v[168:169]
	s_add_i32 m0, s22, 0x2000
	s_nop 0
	global_load_lds_dwordx4 v[180:181], off
	v_lshl_add_u64 v[180:181], v[184:185], 0, s[4:5]
	s_mov_b32 m0, s34
	s_nop 0
	global_load_lds_dwordx4 v[180:181], off
	v_lshl_add_u64 v[180:181], v[186:187], 0, s[4:5]
	s_mov_b32 m0, s35
	s_nop 0
	global_load_lds_dwordx4 v[180:181], off
	s_waitcnt vmcnt(8)
	s_waitcnt lgkmcnt(0)
	s_barrier
	s_setprio 1
	s_waitcnt lgkmcnt(0)
	v_mfma_f32_16x16x128_f8f6f4 v[94:97], v[2:9], v[198:205], v[94:97]
	v_mfma_f32_16x16x128_f8f6f4 v[90:93], v[10:17], v[198:205], v[90:93]
	v_mfma_f32_16x16x128_f8f6f4 v[78:81], v[2:9], v[206:213], v[78:81]
	v_mfma_f32_16x16x128_f8f6f4 v[74:77], v[10:17], v[206:213], v[74:77]
	v_mfma_f32_16x16x128_f8f6f4 v[62:65], v[2:9], v[224:231], v[62:65]
	v_mfma_f32_16x16x128_f8f6f4 v[58:61], v[10:17], v[224:231], v[58:61]
	v_mfma_f32_16x16x128_f8f6f4 v[46:49], v[2:9], v[232:239], v[46:49]
	v_mfma_f32_16x16x128_f8f6f4 v[42:45], v[10:17], v[232:239], v[42:45]
	s_setprio 0
	s_setprio 1
	v_mfma_f32_16x16x128_f8f6f4 v[86:89], v[18:25], v[198:205], v[86:89]
	v_mfma_f32_16x16x128_f8f6f4 v[82:85], v[26:33], v[198:205], v[82:85]
	v_mfma_f32_16x16x128_f8f6f4 v[70:73], v[18:25], v[206:213], v[70:73]
	v_mfma_f32_16x16x128_f8f6f4 v[66:69], v[26:33], v[206:213], v[66:69]
	v_mfma_f32_16x16x128_f8f6f4 v[54:57], v[18:25], v[224:231], v[54:57]
	v_mfma_f32_16x16x128_f8f6f4 v[50:53], v[26:33], v[224:231], v[50:53]
	v_mfma_f32_16x16x128_f8f6f4 v[38:41], v[18:25], v[232:239], v[38:41]
	v_mfma_f32_16x16x128_f8f6f4 v[34:37], v[26:33], v[232:239], v[34:37]
	s_setprio 0
	s_barrier
	s_add_i32 s47, s47, 2
	s_add_u32 s18, s18, 0x100
	s_addc_u32 s19, s19, 0
	s_add_u32 s45, s45, 0x100
	s_addc_u32 s46, s46, 0
	s_cmp_gt_u32 s47, 13
	s_cbranch_scc0 .LBB0_1016
	s_and_b64 vcc, exec, s[6:7]
	s_cbranch_vccz .LBB0_1019
	s_barrier

.LBB0_1098:
	s_ashr_i32 s21, s20, 31
	s_lshl_b64 s[24:25], s[20:21], 19
	s_add_u32 s24, s80, s24
	v_readlane_b32 s3, v254, 41
	s_addc_u32 s25, s3, s25
	s_and_b64 s[8:9], s[8:9], exec
	s_cselect_b32 s3, s25, s27
	s_cselect_b32 s21, s24, s26
	s_add_u32 s8, s28, 0x480080
	s_addc_u32 s9, s29, 0
	s_add_u32 s48, s26, 0x100
	v_mov_b32_e32 v34, 0
	s_addc_u32 s49, s27, 0
	s_mov_b32 s50, -2
	v_mov_b32_e32 v35, v34
	v_mov_b32_e32 v36, v34
	v_mov_b32_e32 v37, v34
	v_mov_b32_e32 v38, v34
	v_mov_b32_e32 v39, v34
	v_mov_b32_e32 v40, v34
	v_mov_b32_e32 v41, v34
	v_mov_b32_e32 v50, v34
	v_mov_b32_e32 v51, v34
	v_mov_b32_e32 v52, v34
	v_mov_b32_e32 v53, v34
	v_mov_b32_e32 v54, v34
	v_mov_b32_e32 v55, v34
	v_mov_b32_e32 v56, v34
	v_mov_b32_e32 v57, v34
	v_mov_b32_e32 v66, v34
	v_mov_b32_e32 v67, v34
	v_mov_b32_e32 v68, v34
	v_mov_b32_e32 v69, v34
	v_mov_b32_e32 v70, v34
	v_mov_b32_e32 v71, v34
	v_mov_b32_e32 v72, v34
	v_mov_b32_e32 v73, v34
	v_mov_b32_e32 v82, v34
	v_mov_b32_e32 v83, v34
	v_mov_b32_e32 v84, v34
	v_mov_b32_e32 v85, v34
	v_mov_b32_e32 v86, v34
	v_mov_b32_e32 v87, v34
	v_mov_b32_e32 v88, v34
	v_mov_b32_e32 v89, v34
	v_mov_b32_e32 v42, v34
	v_mov_b32_e32 v43, v34
	v_mov_b32_e32 v44, v34
	v_mov_b32_e32 v45, v34
	v_mov_b32_e32 v46, v34
	v_mov_b32_e32 v47, v34
	v_mov_b32_e32 v48, v34
	v_mov_b32_e32 v49, v34
	v_mov_b32_e32 v58, v34
	v_mov_b32_e32 v59, v34
	v_mov_b32_e32 v60, v34
	v_mov_b32_e32 v61, v34
	v_mov_b32_e32 v62, v34
	v_mov_b32_e32 v63, v34
	v_mov_b32_e32 v64, v34
	v_mov_b32_e32 v65, v34
	v_mov_b32_e32 v74, v34
	v_mov_b32_e32 v75, v34
	v_mov_b32_e32 v76, v34
	v_mov_b32_e32 v77, v34
	v_mov_b32_e32 v78, v34
	v_mov_b32_e32 v79, v34
	v_mov_b32_e32 v80, v34
	v_mov_b32_e32 v81, v34
	v_mov_b32_e32 v90, v34
	v_mov_b32_e32 v91, v34
	v_mov_b32_e32 v92, v34
	v_mov_b32_e32 v93, v34
	v_mov_b32_e32 v94, v34
	v_mov_b32_e32 v95, v34
	v_mov_b32_e32 v96, v34
	v_mov_b32_e32 v97, v34
	v_mov_b32_e32 v98, v34
	v_mov_b32_e32 v99, v34
	v_mov_b32_e32 v100, v34
	v_mov_b32_e32 v101, v34
	v_mov_b32_e32 v102, v34
	v_mov_b32_e32 v103, v34
	v_mov_b32_e32 v104, v34
	v_mov_b32_e32 v105, v34
	v_mov_b32_e32 v114, v34
	v_mov_b32_e32 v115, v34
	v_mov_b32_e32 v116, v34
	v_mov_b32_e32 v117, v34
	v_mov_b32_e32 v118, v34
	v_mov_b32_e32 v119, v34
	v_mov_b32_e32 v120, v34
	v_mov_b32_e32 v121, v34
	v_mov_b32_e32 v130, v34
	v_mov_b32_e32 v131, v34
	v_mov_b32_e32 v132, v34
	v_mov_b32_e32 v133, v34
	v_mov_b32_e32 v134, v34
	v_mov_b32_e32 v135, v34
	v_mov_b32_e32 v136, v34
	v_mov_b32_e32 v137, v34
	v_mov_b32_e32 v146, v34
	v_mov_b32_e32 v147, v34
	v_mov_b32_e32 v148, v34
	v_mov_b32_e32 v149, v34
	v_mov_b32_e32 v150, v34
	v_mov_b32_e32 v151, v34
	v_mov_b32_e32 v152, v34
	v_mov_b32_e32 v153, v34
	v_mov_b32_e32 v106, v34
	v_mov_b32_e32 v107, v34
	v_mov_b32_e32 v108, v34
	v_mov_b32_e32 v109, v34
	v_mov_b32_e32 v110, v34
	v_mov_b32_e32 v111, v34
	v_mov_b32_e32 v112, v34
	v_mov_b32_e32 v113, v34
	v_mov_b32_e32 v122, v34
	v_mov_b32_e32 v123, v34
	v_mov_b32_e32 v124, v34
	v_mov_b32_e32 v125, v34
	v_mov_b32_e32 v126, v34
	v_mov_b32_e32 v127, v34
	v_mov_b32_e32 v128, v34
	v_mov_b32_e32 v129, v34
	v_mov_b32_e32 v138, v34
	v_mov_b32_e32 v139, v34
	v_mov_b32_e32 v140, v34
	v_mov_b32_e32 v141, v34
	v_mov_b32_e32 v142, v34
	v_mov_b32_e32 v143, v34
	v_mov_b32_e32 v144, v34
	v_mov_b32_e32 v145, v34
	v_mov_b32_e32 v154, v34
	v_mov_b32_e32 v155, v34
	v_mov_b32_e32 v156, v34
	v_mov_b32_e32 v157, v34
	v_mov_b32_e32 v158, v34
	v_mov_b32_e32 v159, v34
	v_mov_b32_e32 v160, v34
	v_mov_b32_e32 v161, v34
.LBB0_1099:
	ds_read_b128 v[26:29], v228
	ds_read_b128 v[30:33], v228 offset:1024
	ds_read_b128 v[18:21], v228 offset:2048
	ds_read_b128 v[22:25], v228 offset:3072
	ds_read_b128 v[10:13], v229
	ds_read_b128 v[14:17], v229 offset:1024
	ds_read_b128 v[2:5], v229 offset:2048
	ds_read_b128 v[6:9], v229 offset:3072
	s_add_u32 s26, s8, 0xffb80080
	s_addc_u32 s27, s9, -1
	s_cmp_eq_u32 s50, 12
	s_cselect_b32 s29, s23, s27
	s_cselect_b32 s28, s22, s26
	s_cselect_b32 s27, s3, s49
	s_cselect_b32 s26, s21, s48
	v_lshl_add_u64 v[208:209], s[8:9], 0, v[188:189]
	s_add_i32 m0, s33, 0xc000
	ds_read_b128 v[162:165], v230
	ds_read_b128 v[166:169], v230 offset:1024
	ds_read_b128 v[170:173], v230 offset:2048
	ds_read_b128 v[174:177], v230 offset:3072
	ds_read_b128 v[192:195], v230 offset:4096
	ds_read_b128 v[196:199], v230 offset:5120
	ds_read_b128 v[200:203], v230 offset:6144
	ds_read_b128 v[204:207], v230 offset:7168
	global_load_lds_dwordx4 v[208:209], off
	v_lshl_add_u64 v[208:209], s[8:9], 0, v[190:191]
	s_add_i32 m0, s33, 0xe000
	s_nop 0
	global_load_lds_dwordx4 v[208:209], off
	s_waitcnt vmcnt(8)
	s_waitcnt lgkmcnt(0)
	s_barrier
	s_setprio 1
	s_waitcnt lgkmcnt(0)
	v_mfma_f32_16x16x128_f8f6f4 v[158:161], v[26:33], v[162:169], v[158:161]
	v_mfma_f32_16x16x128_f8f6f4 v[154:157], v[18:25], v[162:169], v[154:157]
	v_mfma_f32_16x16x128_f8f6f4 v[142:145], v[26:33], v[170:177], v[142:145]
	v_mfma_f32_16x16x128_f8f6f4 v[138:141], v[18:25], v[170:177], v[138:141]
	v_mfma_f32_16x16x128_f8f6f4 v[126:129], v[26:33], v[192:199], v[126:129]
	v_mfma_f32_16x16x128_f8f6f4 v[122:125], v[18:25], v[192:199], v[122:125]
	v_mfma_f32_16x16x128_f8f6f4 v[110:113], v[26:33], v[200:207], v[110:113]
	v_mfma_f32_16x16x128_f8f6f4 v[106:109], v[18:25], v[200:207], v[106:109]
	s_setprio 0
	s_setprio 1
	v_mfma_f32_16x16x128_f8f6f4 v[150:153], v[10:17], v[162:169], v[150:153]
	v_mfma_f32_16x16x128_f8f6f4 v[146:149], v[2:9], v[162:169], v[146:149]
	v_mfma_f32_16x16x128_f8f6f4 v[134:137], v[10:17], v[170:177], v[134:137]
	v_mfma_f32_16x16x128_f8f6f4 v[130:133], v[2:9], v[170:177], v[130:133]
	v_mfma_f32_16x16x128_f8f6f4 v[118:121], v[10:17], v[192:199], v[118:121]
	v_mfma_f32_16x16x128_f8f6f4 v[114:117], v[2:9], v[192:199], v[114:117]
	v_mfma_f32_16x16x128_f8f6f4 v[102:105], v[10:17], v[200:207], v[102:105]
	v_mfma_f32_16x16x128_f8f6f4 v[98:101], v[2:9], v[200:207], v[98:101]
	s_setprio 0
	s_barrier
	s_add_i32 s51, s44, s31
	v_lshl_add_u64 v[162:163], s[26:27], 0, v[182:183]
	s_mov_b32 m0, s51
	ds_read_b128 v[170:173], v230 offset:16384
	ds_read_b128 v[174:177], v230 offset:17408
	ds_read_b128 v[192:195], v230 offset:18432
	ds_read_b128 v[196:199], v230 offset:19456
	ds_read_b128 v[200:203], v230 offset:20480
	ds_read_b128 v[204:207], v230 offset:21504
	ds_read_b128 v[208:211], v230 offset:22528
	ds_read_b128 v[212:215], v230 offset:23552
	global_load_lds_dwordx4 v[162:163], off
	s_add_i32 m0, s51, 0x2000
	s_add_u32 s52, s26, 0x40000
	v_lshl_add_u64 v[164:165], s[26:27], 0, v[186:187]
	s_addc_u32 s53, s27, 0
	s_add_i32 s51, s45, s31
	global_load_lds_dwordx4 v[164:165], off
	v_lshl_add_u64 v[166:167], s[52:53], 0, v[182:183]
	s_mov_b32 m0, s51
	v_lshl_add_u64 v[168:169], s[28:29], 0, v[184:185]
	global_load_lds_dwordx4 v[166:167], off
	v_lshl_add_u64 v[166:167], s[52:53], 0, v[186:187]
	s_add_i32 m0, s51, 0x2000
	s_nop 0
	global_load_lds_dwordx4 v[166:167], off
	v_lshl_add_u64 v[166:167], s[28:29], 0, v[180:181]
	s_mov_b32 m0, s33
	s_nop 0
	global_load_lds_dwordx4 v[166:167], off
	s_mov_b32 m0, s34
	s_nop 0
	global_load_lds_dwordx4 v[168:169], off
	s_waitcnt vmcnt(8)
	s_waitcnt lgkmcnt(0)
	s_barrier
	s_setprio 1
	s_waitcnt lgkmcnt(0)
	v_mfma_f32_16x16x128_f8f6f4 v[94:97], v[26:33], v[170:177], v[94:97]
	v_mfma_f32_16x16x128_f8f6f4 v[90:93], v[18:25], v[170:177], v[90:93]
	v_mfma_f32_16x16x128_f8f6f4 v[78:81], v[26:33], v[192:199], v[78:81]
	v_mfma_f32_16x16x128_f8f6f4 v[74:77], v[18:25], v[192:199], v[74:77]
	v_mfma_f32_16x16x128_f8f6f4 v[62:65], v[26:33], v[200:207], v[62:65]
	v_mfma_f32_16x16x128_f8f6f4 v[58:61], v[18:25], v[200:207], v[58:61]
	v_mfma_f32_16x16x128_f8f6f4 v[46:49], v[26:33], v[208:215], v[46:49]
	v_mfma_f32_16x16x128_f8f6f4 v[42:45], v[18:25], v[208:215], v[42:45]
	s_setprio 0
	s_setprio 1
	v_mfma_f32_16x16x128_f8f6f4 v[86:89], v[10:17], v[170:177], v[86:89]
	v_mfma_f32_16x16x128_f8f6f4 v[82:85], v[2:9], v[170:177], v[82:85]
	v_mfma_f32_16x16x128_f8f6f4 v[70:73], v[10:17], v[192:199], v[70:73]
	v_mfma_f32_16x16x128_f8f6f4 v[66:69], v[2:9], v[192:199], v[66:69]
	v_mfma_f32_16x16x128_f8f6f4 v[54:57], v[10:17], v[200:207], v[54:57]
	v_mfma_f32_16x16x128_f8f6f4 v[50:53], v[2:9], v[200:207], v[50:53]
	v_mfma_f32_16x16x128_f8f6f4 v[38:41], v[10:17], v[208:215], v[38:41]
	v_mfma_f32_16x16x128_f8f6f4 v[34:37], v[2:9], v[208:215], v[34:37]
	s_setprio 0
	s_barrier
	s_add_i32 s51, 0, 0x18000
	s_add_i32 s52, 0, 0x1c000
	v_add_u32_e32 v14, s51, v225
	v_add_u32_e32 v30, s52, v225
	ds_read_b128 v[2:5], v14
	ds_read_b128 v[6:9], v14 offset:1024
	ds_read_b128 v[10:13], v14 offset:2048
	ds_read_b128 v[14:17], v14 offset:3072
	ds_read_b128 v[18:21], v30
	ds_read_b128 v[22:25], v30 offset:1024
	ds_read_b128 v[26:29], v30 offset:2048
	ds_read_b128 v[30:33], v30 offset:3072
	s_add_u32 s28, s28, 0x480000
	s_addc_u32 s29, s29, 0
	s_mov_b32 m0, s35
	v_lshl_add_u64 v[216:217], s[28:29], 0, v[180:181]
	ds_read_b128 v[170:173], v230 offset:32768
	ds_read_b128 v[174:177], v230 offset:33792
	ds_read_b128 v[192:195], v230 offset:34816
	ds_read_b128 v[196:199], v230 offset:35840
	ds_read_b128 v[200:203], v230 offset:36864
	ds_read_b128 v[204:207], v230 offset:37888
	ds_read_b128 v[208:211], v230 offset:38912
	ds_read_b128 v[212:215], v230 offset:39936
	global_load_lds_dwordx4 v[216:217], off
	v_lshl_add_u64 v[216:217], s[28:29], 0, v[184:185]
	s_mov_b32 m0, s36
	s_nop 0
	global_load_lds_dwordx4 v[216:217], off
	s_waitcnt vmcnt(8)
	s_waitcnt lgkmcnt(0)
	s_barrier
	s_setprio 1
	s_waitcnt lgkmcnt(0)
	v_mfma_f32_16x16x128_f8f6f4 v[158:161], v[2:9], v[170:177], v[158:161]
	v_mfma_f32_16x16x128_f8f6f4 v[154:157], v[10:17], v[170:177], v[154:157]
	v_mfma_f32_16x16x128_f8f6f4 v[142:145], v[2:9], v[192:199], v[142:145]
	v_mfma_f32_16x16x128_f8f6f4 v[138:141], v[10:17], v[192:199], v[138:141]
	v_mfma_f32_16x16x128_f8f6f4 v[126:129], v[2:9], v[200:207], v[126:129]
	v_mfma_f32_16x16x128_f8f6f4 v[122:125], v[10:17], v[200:207], v[122:125]
	v_mfma_f32_16x16x128_f8f6f4 v[110:113], v[2:9], v[208:215], v[110:113]
	v_mfma_f32_16x16x128_f8f6f4 v[106:109], v[10:17], v[208:215], v[106:109]
	s_setprio 0
	s_setprio 1
	v_mfma_f32_16x16x128_f8f6f4 v[150:153], v[18:25], v[170:177], v[150:153]
	v_mfma_f32_16x16x128_f8f6f4 v[146:149], v[26:33], v[170:177], v[146:149]
	v_mfma_f32_16x16x128_f8f6f4 v[134:137], v[18:25], v[192:199], v[134:137]
	v_mfma_f32_16x16x128_f8f6f4 v[130:133], v[26:33], v[192:199], v[130:133]
	v_mfma_f32_16x16x128_f8f6f4 v[118:121], v[18:25], v[200:207], v[118:121]
	v_mfma_f32_16x16x128_f8f6f4 v[114:117], v[26:33], v[200:207], v[114:117]
	v_mfma_f32_16x16x128_f8f6f4 v[102:105], v[18:25], v[208:215], v[102:105]
	v_mfma_f32_16x16x128_f8f6f4 v[98:101], v[26:33], v[208:215], v[98:101]
	s_setprio 0
	s_barrier
	s_add_i32 s28, s51, s31
	v_lshl_add_u64 v[162:163], v[162:163], 0, s[12:13]
	s_mov_b32 m0, s28
	ds_read_b128 v[170:173], v230 offset:49152
	ds_read_b128 v[174:177], v230 offset:50176
	ds_read_b128 v[192:195], v230 offset:51200
	ds_read_b128 v[196:199], v230 offset:52224
	ds_read_b128 v[200:203], v230 offset:53248
	ds_read_b128 v[204:207], v230 offset:54272
	ds_read_b128 v[208:211], v230 offset:55296
	ds_read_b128 v[212:215], v230 offset:56320
	global_load_lds_dwordx4 v[162:163], off
	s_add_i32 m0, s28, 0x2000
	s_add_u32 s26, s26, 0x40080
	v_lshl_add_u64 v[162:163], v[164:165], 0, s[12:13]
	s_addc_u32 s27, s27, 0
	s_add_i32 s28, s52, s31
	global_load_lds_dwordx4 v[162:163], off
	v_lshl_add_u64 v[162:163], s[26:27], 0, v[182:183]
	s_mov_b32 m0, s28
	s_nop 0
	global_load_lds_dwordx4 v[162:163], off
	v_lshl_add_u64 v[162:163], s[26:27], 0, v[186:187]
	s_add_i32 m0, s28, 0x2000
	s_nop 0
	global_load_lds_dwordx4 v[162:163], off
	v_lshl_add_u64 v[162:163], v[166:167], 0, s[12:13]
	s_mov_b32 m0, s40
	s_nop 0
	global_load_lds_dwordx4 v[162:163], off
	v_lshl_add_u64 v[162:163], v[168:169], 0, s[12:13]
	s_mov_b32 m0, s41
	s_nop 0
	global_load_lds_dwordx4 v[162:163], off
	s_waitcnt vmcnt(8)
	s_waitcnt lgkmcnt(0)
	s_barrier
	s_setprio 1
	s_waitcnt lgkmcnt(0)
	v_mfma_f32_16x16x128_f8f6f4 v[94:97], v[2:9], v[170:177], v[94:97]
	v_mfma_f32_16x16x128_f8f6f4 v[90:93], v[10:17], v[170:177], v[90:93]
	v_mfma_f32_16x16x128_f8f6f4 v[78:81], v[2:9], v[192:199], v[78:81]
	v_mfma_f32_16x16x128_f8f6f4 v[74:77], v[10:17], v[192:199], v[74:77]
	v_mfma_f32_16x16x128_f8f6f4 v[62:65], v[2:9], v[200:207], v[62:65]
	v_mfma_f32_16x16x128_f8f6f4 v[58:61], v[10:17], v[200:207], v[58:61]
	v_mfma_f32_16x16x128_f8f6f4 v[46:49], v[2:9], v[208:215], v[46:49]
	v_mfma_f32_16x16x128_f8f6f4 v[42:45], v[10:17], v[208:215], v[42:45]
	s_setprio 0
	s_setprio 1
	v_mfma_f32_16x16x128_f8f6f4 v[86:89], v[18:25], v[170:177], v[86:89]
	v_mfma_f32_16x16x128_f8f6f4 v[82:85], v[26:33], v[170:177], v[82:85]
	v_mfma_f32_16x16x128_f8f6f4 v[70:73], v[18:25], v[192:199], v[70:73]
	v_mfma_f32_16x16x128_f8f6f4 v[66:69], v[26:33], v[192:199], v[66:69]
	v_mfma_f32_16x16x128_f8f6f4 v[54:57], v[18:25], v[200:207], v[54:57]
	v_mfma_f32_16x16x128_f8f6f4 v[50:53], v[26:33], v[200:207], v[50:53]
	v_mfma_f32_16x16x128_f8f6f4 v[38:41], v[18:25], v[208:215], v[38:41]
	v_mfma_f32_16x16x128_f8f6f4 v[34:37], v[26:33], v[208:215], v[34:37]
	s_setprio 0
	s_barrier
	s_add_i32 s50, s50, 2
	s_add_u32 s8, s8, 0x100
	s_addc_u32 s9, s9, 0
	s_add_u32 s48, s48, 0x100
	s_addc_u32 s49, s49, 0
	s_cmp_gt_u32 s50, 13
	s_cbranch_scc0 .LBB0_1099
	s_and_b64 vcc, exec, s[14:15]
	s_cbranch_vccz .LBB0_1102
	s_barrier
